# v56 + local hand-offs: L1 invalidate issued right after the arrive (before polling) so its latency hides under the wait
# baseline (speedup 1.0000x reference)
; __device__ __forceinline__ unsigned xb_ld(unsigned* p)              { return __hip_atomic_load(p, __ATOMIC_RELAXED, __HIP_MEMORY_SCOPE_AGENT); }
; __device__ __forceinline__ unsigned xb_add(unsigned* p, unsigned v) { return __hip_atomic_fetch_add(p, v, __ATOMIC_RELAXED, __HIP_MEMORY_SCOPE_AGENT); }
; #define XB_SPIN(cond, bar) do { unsigned _sp = 0; while (cond) { __builtin_amdgcn_s_sleep(1); \
;     if ((++_sp & 255u) == 0u) { if (xb_ld(&(bar)[XB_TMO])) break; if (_sp > XB_SPIN_CAP) { atomicAdd(&(bar)[XB_TMO], 1u); break; } } } } while (0)
; __device__ __forceinline__ void xcd_barrier(const XcdBarrier& b) {
;     asm volatile("s_waitcnt vmcnt(0)" ::: "memory");
;     __syncthreads();
;     if (threadIdx.x == 0) {
;         unsigned* bar = b.bar;
;         __builtin_amdgcn_s_waitcnt(0);
;         unsigned nloc = b.st[0], nx = b.st[1];
;         if (nloc == 0u) { xcd_barrier_complete(bar, b.x, nloc, nx); b.st[0] = nloc; b.st[1] = nx; }
;         const unsigned old = xb_add(&bar[XB_XSUB(b.x)], 1u);
;         const unsigned gen = old / nloc;
;         if (old + 1u == (gen + 1u) * nloc) {
;             __builtin_amdgcn_fence(__ATOMIC_RELEASE, "agent");
;             asm volatile("s_waitcnt vmcnt(0)" ::: "memory");
;             const unsigned og = xb_add(&bar[XB_TOP], 1u);
;             const unsigned tg = og / nx;
;             if (og + 1u == (tg + 1u) * nx) xb_add(&bar[XB_TOPGEN], 1u);
;             else XB_SPIN(xb_ld(&bar[XB_TOPGEN]) == tg, bar);
;             __builtin_amdgcn_fence(__ATOMIC_ACQUIRE, "agent");
;             xb_add(&bar[XB_XGEN(b.x)], 1u);
;             asm volatile("s_waitcnt vmcnt(0)" ::: "memory");
;         } else {
;             XB_SPIN(xb_ld(&bar[XB_XGEN(b.x)]) == gen, bar);
;             __builtin_amdgcn_fence(__ATOMIC_ACQUIRE, "agent");
;             asm volatile("s_waitcnt vmcnt(0)" ::: "memory");
;         }
;     }
;     __syncthreads();
.LBB0_599:
	v_readlane_b32 s0, v253, 42
	v_readlane_b32 s4, v253, 32
	s_add_i32 s0, s0, 1
	v_readlane_b32 s7, v253, 35
	s_cmp_ge_i32 s0, s7
	v_readlane_b32 s5, v253, 33
	v_readlane_b32 s6, v253, 34
	s_cbranch_scc1 .LBB0_645
	v_readlane_b32 s34, v253, 36
	v_readlane_b32 s35, v253, 37
	s_mov_b32 s1, s76
	s_waitcnt vmcnt(0)
	s_waitcnt vmcnt(0) lgkmcnt(0)
	s_barrier
	s_mov_b64 s[40:41], exec
	v_readlane_b32 s2, v253, 53
	v_readlane_b32 s3, v253, 54
	s_and_b64 s[2:3], s[40:41], s[2:3]
	s_mov_b64 exec, s[2:3]
	s_cbranch_execz .LBB0_644
	v_readlane_b32 s10, v253, 36
	v_readlane_b32 s11, v253, 37
	v_readlane_b32 s14, v253, 55
	s_nop 3
	s_add_u32 s12, s10, 0x5000
	s_addc_u32 s13, s11, 0
	s_and_b32 s15, s88, 7
	s_lshr_b32 s16, s88, 3
	s_lshl_b32 s15, s15, 3
	s_and_b32 s17, s16, 7
	s_add_i32 s17, s17, s15
	s_lshr_b32 s16, s16, 2
	s_add_i32 s16, s16, s15
	s_lshl_b32 s17, s17, 6
	s_lshl_b32 s16, s16, 6
	s_mov_b32 s16, s17
	s_add_i32 s14, s14, 1
	s_lshl_b32 s14, s14, 2
	v_mov_b32_e32 v2, s17
	v_mov_b32_e32 v5, 1
	v_mov_b32_e32 v4, s16
	global_atomic_add v2, v5, s[12:13]
	buffer_inv sc1
	s_mov_b32 s18, 0
.Lth_poll_LBB0_644:
	global_load_dword v6, v4, s[12:13] sc1
	s_waitcnt vmcnt(0)
	v_cmp_gt_u32_e32 vcc, s14, v6
	s_nop 3
	s_cmp_eq_u64 vcc, 0
	s_cbranch_scc1 .Lth_done_LBB0_644
	s_add_i32 s18, s18, 1
	s_cmp_gt_u32 s18, 0x4000
	s_cbranch_scc1 .Lth_done_LBB0_644
	s_sleep 1
	s_branch .Lth_poll_LBB0_644
.Lth_done_LBB0_644:
	s_waitcnt vmcnt(0)
.LBB0_644:
	s_or_b64 exec, exec, s[40:41]
	s_waitcnt lgkmcnt(0)
	s_barrier

; __device__ __forceinline__ unsigned xb_ld(unsigned* p)              { return __hip_atomic_load(p, __ATOMIC_RELAXED, __HIP_MEMORY_SCOPE_AGENT); }
; __device__ __forceinline__ unsigned xb_add(unsigned* p, unsigned v) { return __hip_atomic_fetch_add(p, v, __ATOMIC_RELAXED, __HIP_MEMORY_SCOPE_AGENT); }
; #define XB_SPIN(cond, bar) do { unsigned _sp = 0; while (cond) { __builtin_amdgcn_s_sleep(1); \
;     if ((++_sp & 255u) == 0u) { if (xb_ld(&(bar)[XB_TMO])) break; if (_sp > XB_SPIN_CAP) { atomicAdd(&(bar)[XB_TMO], 1u); break; } } } } while (0)
; __device__ __forceinline__ void xcd_barrier(const XcdBarrier& b) {
;     asm volatile("s_waitcnt vmcnt(0)" ::: "memory");
;     __syncthreads();
;     if (threadIdx.x == 0) {
;         unsigned* bar = b.bar;
;         __builtin_amdgcn_s_waitcnt(0);
;         unsigned nloc = b.st[0], nx = b.st[1];
;         if (nloc == 0u) { xcd_barrier_complete(bar, b.x, nloc, nx); b.st[0] = nloc; b.st[1] = nx; }
;         const unsigned old = xb_add(&bar[XB_XSUB(b.x)], 1u);
;         const unsigned gen = old / nloc;
;         if (old + 1u == (gen + 1u) * nloc) {
;             __builtin_amdgcn_fence(__ATOMIC_RELEASE, "agent");
;             asm volatile("s_waitcnt vmcnt(0)" ::: "memory");
;             const unsigned og = xb_add(&bar[XB_TOP], 1u);
;             const unsigned tg = og / nx;
;             if (og + 1u == (tg + 1u) * nx) xb_add(&bar[XB_TOPGEN], 1u);
;             else XB_SPIN(xb_ld(&bar[XB_TOPGEN]) == tg, bar);
;             __builtin_amdgcn_fence(__ATOMIC_ACQUIRE, "agent");
;             xb_add(&bar[XB_XGEN(b.x)], 1u);
;             asm volatile("s_waitcnt vmcnt(0)" ::: "memory");
;         } else {
;             XB_SPIN(xb_ld(&bar[XB_XGEN(b.x)]) == gen, bar);
;             __builtin_amdgcn_fence(__ATOMIC_ACQUIRE, "agent");
;             asm volatile("s_waitcnt vmcnt(0)" ::: "memory");
;         }
;     }
;     __syncthreads();
.LBB0_676:
	v_readlane_b32 s0, v253, 42
	v_readlane_b32 s4, v253, 32
	s_add_i32 s0, s0, 2
	v_readlane_b32 s7, v253, 35
	s_cmp_ge_i32 s0, s7
	v_readlane_b32 s5, v253, 33
	v_readlane_b32 s6, v253, 34
	s_cbranch_scc1 .LBB0_722
	v_readlane_b32 s34, v253, 36
	v_readlane_b32 s35, v253, 37
	s_mov_b32 s1, s76
	s_waitcnt vmcnt(0)
	s_waitcnt vmcnt(0) lgkmcnt(0)
	s_barrier
	s_mov_b64 s[40:41], exec
	v_readlane_b32 s2, v253, 53
	v_readlane_b32 s3, v253, 54
	s_and_b64 s[2:3], s[40:41], s[2:3]
	s_mov_b64 exec, s[2:3]
	s_cbranch_execz .LBB0_721
	v_readlane_b32 s10, v253, 36
	v_readlane_b32 s11, v253, 37
	v_readlane_b32 s14, v253, 55
	s_nop 3
	s_add_u32 s12, s10, 0x4000
	s_addc_u32 s13, s11, 0
	s_and_b32 s15, s88, 7
	s_lshr_b32 s16, s88, 3
	s_lshl_b32 s15, s15, 3
	s_and_b32 s17, s16, 7
	s_add_i32 s17, s17, s15
	s_lshr_b32 s16, s16, 2
	s_add_i32 s16, s16, s15
	s_lshl_b32 s17, s17, 6
	s_lshl_b32 s16, s16, 6
	s_add_i32 s14, s14, 1
	s_lshl_b32 s14, s14, 2
	v_mov_b32_e32 v2, s17
	v_mov_b32_e32 v5, 1
	v_mov_b32_e32 v4, s16
	global_atomic_add v2, v5, s[12:13]
	buffer_inv sc1
	s_mov_b32 s18, 0
.Lth_poll_LBB0_721:
	global_load_dword v6, v4, s[12:13] sc1
	s_waitcnt vmcnt(0)
	v_cmp_gt_u32_e32 vcc, s14, v6
	s_nop 3
	s_cmp_eq_u64 vcc, 0
	s_cbranch_scc1 .Lth_done_LBB0_721
	s_add_i32 s18, s18, 1
	s_cmp_gt_u32 s18, 0x4000
	s_cbranch_scc1 .Lth_done_LBB0_721
	s_sleep 1
	s_branch .Lth_poll_LBB0_721
.Lth_done_LBB0_721:
	s_waitcnt vmcnt(0)
.LBB0_721:
	s_or_b64 exec, exec, s[40:41]
	s_waitcnt lgkmcnt(0)
	s_barrier

; __device__ __forceinline__ unsigned xb_ld(unsigned* p)              { return __hip_atomic_load(p, __ATOMIC_RELAXED, __HIP_MEMORY_SCOPE_AGENT); }
; __device__ __forceinline__ unsigned xb_add(unsigned* p, unsigned v) { return __hip_atomic_fetch_add(p, v, __ATOMIC_RELAXED, __HIP_MEMORY_SCOPE_AGENT); }
; #define XB_SPIN(cond, bar) do { unsigned _sp = 0; while (cond) { __builtin_amdgcn_s_sleep(1); \
;     if ((++_sp & 255u) == 0u) { if (xb_ld(&(bar)[XB_TMO])) break; if (_sp > XB_SPIN_CAP) { atomicAdd(&(bar)[XB_TMO], 1u); break; } } } } while (0)
; __device__ __forceinline__ void xcd_barrier(const XcdBarrier& b) {
;     asm volatile("s_waitcnt vmcnt(0)" ::: "memory");
;     __syncthreads();
;     if (threadIdx.x == 0) {
;         unsigned* bar = b.bar;
;         __builtin_amdgcn_s_waitcnt(0);
;         unsigned nloc = b.st[0], nx = b.st[1];
;         if (nloc == 0u) { xcd_barrier_complete(bar, b.x, nloc, nx); b.st[0] = nloc; b.st[1] = nx; }
;         const unsigned old = xb_add(&bar[XB_XSUB(b.x)], 1u);
;         const unsigned gen = old / nloc;
;         if (old + 1u == (gen + 1u) * nloc) {
;             __builtin_amdgcn_fence(__ATOMIC_RELEASE, "agent");
;             asm volatile("s_waitcnt vmcnt(0)" ::: "memory");
;             const unsigned og = xb_add(&bar[XB_TOP], 1u);
;             const unsigned tg = og / nx;
;             if (og + 1u == (tg + 1u) * nx) xb_add(&bar[XB_TOPGEN], 1u);
;             else XB_SPIN(xb_ld(&bar[XB_TOPGEN]) == tg, bar);
;             __builtin_amdgcn_fence(__ATOMIC_ACQUIRE, "agent");
;             xb_add(&bar[XB_XGEN(b.x)], 1u);
;             asm volatile("s_waitcnt vmcnt(0)" ::: "memory");
;         } else {
;             XB_SPIN(xb_ld(&bar[XB_XGEN(b.x)]) == gen, bar);
;             __builtin_amdgcn_fence(__ATOMIC_ACQUIRE, "agent");
;             asm volatile("s_waitcnt vmcnt(0)" ::: "memory");
;         }
;     }
;     __syncthreads();
.LBB0_1027:
	v_readlane_b32 s0, v253, 42
	v_readlane_b32 s4, v253, 32
	s_add_i32 s0, s0, 5
	v_readlane_b32 s7, v253, 35
	s_cmp_ge_i32 s0, s7
	v_readlane_b32 s5, v253, 33
	v_readlane_b32 s6, v253, 34
	s_cbranch_scc1 .LBB0_1073
	v_readlane_b32 s38, v253, 36
	v_readlane_b32 s39, v253, 37
	s_mov_b32 s1, s76
	s_waitcnt vmcnt(0)
	s_waitcnt vmcnt(0)
	s_barrier
	s_mov_b64 s[40:41], exec
	v_readlane_b32 s4, v253, 53
	v_readlane_b32 s5, v253, 54
	s_and_b64 s[4:5], s[40:41], s[4:5]
	s_mov_b64 exec, s[4:5]
	s_cbranch_execz .LBB0_1072
	v_readlane_b32 s10, v253, 36
	v_readlane_b32 s11, v253, 37
	v_readlane_b32 s14, v253, 55
	s_nop 3
	s_add_u32 s12, s10, 0x8000
	s_addc_u32 s13, s11, 0
	s_and_b32 s15, s88, 7
	s_lshl_b32 s15, s15, 8
	s_lshr_b32 s14, s14, 2
	s_add_i32 s14, s14, 1
	s_lshl_b32 s14, s14, 5
	v_mov_b32_e32 v2, s15
	v_mov_b32_e32 v5, 1
	global_atomic_add v2, v5, s[12:13]
	buffer_inv sc1
	s_mov_b32 s18, 0
.Lgh_poll_LBB0_1072:
	global_load_dword v6, v2, s[12:13] sc1
	s_waitcnt vmcnt(0)
	v_cmp_gt_u32_e32 vcc, s14, v6
	s_nop 3
	s_cmp_eq_u64 vcc, 0
	s_cbranch_scc1 .Lgh_done_LBB0_1072
	s_add_i32 s18, s18, 1
	s_cmp_gt_u32 s18, 0x4000
	s_cbranch_scc1 .Lgh_done_LBB0_1072
	s_sleep 1
	s_branch .Lgh_poll_LBB0_1072
.Lgh_done_LBB0_1072:
	s_waitcnt vmcnt(0)
.LBB0_1072:
	s_or_b64 exec, exec, s[40:41]
	s_waitcnt lgkmcnt(0)
	s_barrier

; __device__ __forceinline__ unsigned xb_ld(unsigned* p)              { return __hip_atomic_load(p, __ATOMIC_RELAXED, __HIP_MEMORY_SCOPE_AGENT); }
; __device__ __forceinline__ unsigned xb_add(unsigned* p, unsigned v) { return __hip_atomic_fetch_add(p, v, __ATOMIC_RELAXED, __HIP_MEMORY_SCOPE_AGENT); }
; #define XB_SPIN(cond, bar) do { unsigned _sp = 0; while (cond) { __builtin_amdgcn_s_sleep(1); \
;     if ((++_sp & 255u) == 0u) { if (xb_ld(&(bar)[XB_TMO])) break; if (_sp > XB_SPIN_CAP) { atomicAdd(&(bar)[XB_TMO], 1u); break; } } } } while (0)
; __device__ __forceinline__ void xcd_barrier(const XcdBarrier& b) {
;     asm volatile("s_waitcnt vmcnt(0)" ::: "memory");
;     __syncthreads();
;     if (threadIdx.x == 0) {
;         unsigned* bar = b.bar;
;         __builtin_amdgcn_s_waitcnt(0);
;         unsigned nloc = b.st[0], nx = b.st[1];
;         if (nloc == 0u) { xcd_barrier_complete(bar, b.x, nloc, nx); b.st[0] = nloc; b.st[1] = nx; }
;         const unsigned old = xb_add(&bar[XB_XSUB(b.x)], 1u);
;         const unsigned gen = old / nloc;
;         if (old + 1u == (gen + 1u) * nloc) {
;             __builtin_amdgcn_fence(__ATOMIC_RELEASE, "agent");
;             asm volatile("s_waitcnt vmcnt(0)" ::: "memory");
;             const unsigned og = xb_add(&bar[XB_TOP], 1u);
;             const unsigned tg = og / nx;
;             if (og + 1u == (tg + 1u) * nx) xb_add(&bar[XB_TOPGEN], 1u);
;             else XB_SPIN(xb_ld(&bar[XB_TOPGEN]) == tg, bar);
;             __builtin_amdgcn_fence(__ATOMIC_ACQUIRE, "agent");
;             xb_add(&bar[XB_XGEN(b.x)], 1u);
;             asm volatile("s_waitcnt vmcnt(0)" ::: "memory");
;         } else {
;             XB_SPIN(xb_ld(&bar[XB_XGEN(b.x)]) == gen, bar);
;             __builtin_amdgcn_fence(__ATOMIC_ACQUIRE, "agent");
;             asm volatile("s_waitcnt vmcnt(0)" ::: "memory");
;         }
;     }
;     __syncthreads();
.LBB0_1100:
	v_readlane_b32 s0, v253, 42
	v_readlane_b32 s4, v253, 32
	s_add_i32 s0, s0, 6
	v_readlane_b32 s7, v253, 35
	s_cmp_ge_i32 s0, s7
	v_readlane_b32 s5, v253, 33
	v_readlane_b32 s6, v253, 34
	s_cbranch_scc1 .LBB0_1146
	v_readlane_b32 s38, v253, 36
	v_readlane_b32 s39, v253, 37
	s_mov_b32 s1, s76
	s_waitcnt vmcnt(0)
	s_waitcnt vmcnt(0) lgkmcnt(0)
	s_barrier
	s_mov_b64 s[40:41], exec
	v_readlane_b32 s4, v253, 53
	v_readlane_b32 s5, v253, 54
	s_and_b64 s[4:5], s[40:41], s[4:5]
	s_mov_b64 exec, s[4:5]
	s_cbranch_execz .LBB0_1145
	v_readlane_b32 s10, v253, 36
	v_readlane_b32 s11, v253, 37
	v_readlane_b32 s14, v253, 55
	s_nop 3
	s_add_u32 s12, s10, 0x6000
	s_addc_u32 s13, s11, 0
	s_and_b32 s15, s88, 7
	s_lshr_b32 s16, s88, 3
	s_lshl_b32 s15, s15, 3
	s_and_b32 s17, s16, 7
	s_add_i32 s17, s17, s15
	s_lshr_b32 s16, s16, 2
	s_add_i32 s16, s16, s15
	s_lshl_b32 s17, s17, 6
	s_lshl_b32 s16, s16, 6
	s_lshr_b32 s14, s14, 1
	s_add_i32 s14, s14, 1
	s_lshl_b32 s14, s14, 2
	v_mov_b32_e32 v2, s17
	v_mov_b32_e32 v5, 1
	v_mov_b32_e32 v4, s16
	global_atomic_add v2, v5, s[12:13]
	buffer_inv sc1
	s_mov_b32 s18, 0
.Lth_poll_LBB0_1145:
	global_load_dword v6, v4, s[12:13] sc1
	s_waitcnt vmcnt(0)
	v_cmp_gt_u32_e32 vcc, s14, v6
	s_nop 3
	s_cmp_eq_u64 vcc, 0
	s_cbranch_scc1 .Lth_done_LBB0_1145
	s_add_i32 s18, s18, 1
	s_cmp_gt_u32 s18, 0x4000
	s_cbranch_scc1 .Lth_done_LBB0_1145
	s_sleep 1
	s_branch .Lth_poll_LBB0_1145
.Lth_done_LBB0_1145:
	s_waitcnt vmcnt(0)
.LBB0_1145:
	s_or_b64 exec, exec, s[40:41]
	s_waitcnt lgkmcnt(0)
	s_barrier

; __device__ __forceinline__ unsigned xb_ld(unsigned* p)              { return __hip_atomic_load(p, __ATOMIC_RELAXED, __HIP_MEMORY_SCOPE_AGENT); }
; __device__ __forceinline__ unsigned xb_add(unsigned* p, unsigned v) { return __hip_atomic_fetch_add(p, v, __ATOMIC_RELAXED, __HIP_MEMORY_SCOPE_AGENT); }
; #define XB_SPIN(cond, bar) do { unsigned _sp = 0; while (cond) { __builtin_amdgcn_s_sleep(1); \
;     if ((++_sp & 255u) == 0u) { if (xb_ld(&(bar)[XB_TMO])) break; if (_sp > XB_SPIN_CAP) { atomicAdd(&(bar)[XB_TMO], 1u); break; } } } } while (0)
; __device__ __forceinline__ void xcd_barrier(const XcdBarrier& b) {
;     asm volatile("s_waitcnt vmcnt(0)" ::: "memory");
;     __syncthreads();
;     if (threadIdx.x == 0) {
;         unsigned* bar = b.bar;
;         __builtin_amdgcn_s_waitcnt(0);
;         unsigned nloc = b.st[0], nx = b.st[1];
;         if (nloc == 0u) { xcd_barrier_complete(bar, b.x, nloc, nx); b.st[0] = nloc; b.st[1] = nx; }
;         const unsigned old = xb_add(&bar[XB_XSUB(b.x)], 1u);
;         const unsigned gen = old / nloc;
;         if (old + 1u == (gen + 1u) * nloc) {
;             __builtin_amdgcn_fence(__ATOMIC_RELEASE, "agent");
;             asm volatile("s_waitcnt vmcnt(0)" ::: "memory");
;             const unsigned og = xb_add(&bar[XB_TOP], 1u);
;             const unsigned tg = og / nx;
;             if (og + 1u == (tg + 1u) * nx) xb_add(&bar[XB_TOPGEN], 1u);
;             else XB_SPIN(xb_ld(&bar[XB_TOPGEN]) == tg, bar);
;             __builtin_amdgcn_fence(__ATOMIC_ACQUIRE, "agent");
;             xb_add(&bar[XB_XGEN(b.x)], 1u);
;             asm volatile("s_waitcnt vmcnt(0)" ::: "memory");
;         } else {
;             XB_SPIN(xb_ld(&bar[XB_XGEN(b.x)]) == gen, bar);
;             __builtin_amdgcn_fence(__ATOMIC_ACQUIRE, "agent");
;             asm volatile("s_waitcnt vmcnt(0)" ::: "memory");
;         }
;     }
;     __syncthreads();
.LBB0_1627:
	v_readlane_b32 s0, v253, 42
	v_readlane_b32 s4, v253, 32
	s_add_i32 s0, s0, 7
	v_readlane_b32 s7, v253, 35
	s_cmp_ge_i32 s0, s7
	v_readlane_b32 s5, v253, 33
	v_readlane_b32 s6, v253, 34
	s_cbranch_scc1 .LBB0_1673
	v_readlane_b32 s34, v253, 36
	v_readlane_b32 s35, v253, 37
	s_mov_b32 s1, s76
	s_waitcnt vmcnt(0)
	s_waitcnt vmcnt(0) lgkmcnt(0)
	s_barrier
	s_mov_b64 s[36:37], exec
	v_readlane_b32 s2, v253, 53
	v_readlane_b32 s3, v253, 54
	s_and_b64 s[2:3], s[36:37], s[2:3]
	s_mov_b64 exec, s[2:3]
	s_cbranch_execz .LBB0_1672
	v_readlane_b32 s10, v253, 36
	v_readlane_b32 s11, v253, 37
	v_readlane_b32 s14, v253, 55
	s_nop 3
	s_add_u32 s12, s10, 0x8800
	s_addc_u32 s13, s11, 0
	s_and_b32 s15, s88, 7
	s_lshl_b32 s15, s15, 8
	s_lshr_b32 s14, s14, 2
	s_add_i32 s14, s14, 1
	s_lshl_b32 s14, s14, 5
	v_mov_b32_e32 v2, s15
	v_mov_b32_e32 v5, 1
	global_atomic_add v2, v5, s[12:13]
	buffer_inv sc1
	s_mov_b32 s18, 0
.Lgh_poll_LBB0_1672:
	global_load_dword v6, v2, s[12:13] sc1
	s_waitcnt vmcnt(0)
	v_cmp_gt_u32_e32 vcc, s14, v6
	s_nop 3
	s_cmp_eq_u64 vcc, 0
	s_cbranch_scc1 .Lgh_done_LBB0_1672
	s_add_i32 s18, s18, 1
	s_cmp_gt_u32 s18, 0x4000
	s_cbranch_scc1 .Lgh_done_LBB0_1672
	s_sleep 1
	s_branch .Lgh_poll_LBB0_1672
.Lgh_done_LBB0_1672:
	s_waitcnt vmcnt(0)
.LBB0_1672:
	s_or_b64 exec, exec, s[36:37]
	s_waitcnt lgkmcnt(0)
	s_barrier

; __device__ __forceinline__ unsigned xb_ld(unsigned* p)              { return __hip_atomic_load(p, __ATOMIC_RELAXED, __HIP_MEMORY_SCOPE_AGENT); }
; __device__ __forceinline__ unsigned xb_add(unsigned* p, unsigned v) { return __hip_atomic_fetch_add(p, v, __ATOMIC_RELAXED, __HIP_MEMORY_SCOPE_AGENT); }
; #define XB_SPIN(cond, bar) do { unsigned _sp = 0; while (cond) { __builtin_amdgcn_s_sleep(1); \
;     if ((++_sp & 255u) == 0u) { if (xb_ld(&(bar)[XB_TMO])) break; if (_sp > XB_SPIN_CAP) { atomicAdd(&(bar)[XB_TMO], 1u); break; } } } } while (0)
; __device__ __forceinline__ void xcd_barrier(const XcdBarrier& b) {
;     asm volatile("s_waitcnt vmcnt(0)" ::: "memory");
;     __syncthreads();
;     if (threadIdx.x == 0) {
;         unsigned* bar = b.bar;
;         __builtin_amdgcn_s_waitcnt(0);
;         unsigned nloc = b.st[0], nx = b.st[1];
;         if (nloc == 0u) { xcd_barrier_complete(bar, b.x, nloc, nx); b.st[0] = nloc; b.st[1] = nx; }
;         const unsigned old = xb_add(&bar[XB_XSUB(b.x)], 1u);
;         const unsigned gen = old / nloc;
;         if (old + 1u == (gen + 1u) * nloc) {
;             __builtin_amdgcn_fence(__ATOMIC_RELEASE, "agent");
;             asm volatile("s_waitcnt vmcnt(0)" ::: "memory");
;             const unsigned og = xb_add(&bar[XB_TOP], 1u);
;             const unsigned tg = og / nx;
;             if (og + 1u == (tg + 1u) * nx) xb_add(&bar[XB_TOPGEN], 1u);
;             else XB_SPIN(xb_ld(&bar[XB_TOPGEN]) == tg, bar);
;             __builtin_amdgcn_fence(__ATOMIC_ACQUIRE, "agent");
;             xb_add(&bar[XB_XGEN(b.x)], 1u);
;             asm volatile("s_waitcnt vmcnt(0)" ::: "memory");
;         } else {
;             XB_SPIN(xb_ld(&bar[XB_XGEN(b.x)]) == gen, bar);
;             __builtin_amdgcn_fence(__ATOMIC_ACQUIRE, "agent");
;             asm volatile("s_waitcnt vmcnt(0)" ::: "memory");
;         }
;     }
;     __syncthreads();
.LBB0_1700:
	v_readlane_b32 s0, v253, 42
	v_readlane_b32 s4, v253, 32
	s_add_i32 s0, s0, 8
	v_readlane_b32 s7, v253, 35
	s_cmp_ge_i32 s0, s7
	v_readlane_b32 s5, v253, 33
	v_readlane_b32 s6, v253, 34
	s_cbranch_scc1 .LBB0_1746
	v_readlane_b32 s34, v253, 36
	v_readlane_b32 s35, v253, 37
	s_mov_b32 s1, s76
	s_waitcnt vmcnt(0)
	s_waitcnt vmcnt(0) lgkmcnt(0)
	s_barrier
	s_mov_b64 s[36:37], exec
	v_readlane_b32 s2, v253, 53
	v_readlane_b32 s3, v253, 54
	s_and_b64 s[2:3], s[36:37], s[2:3]
	s_mov_b64 exec, s[2:3]
	s_cbranch_execz .LBB0_1745
	v_readlane_b32 s10, v253, 36
	v_readlane_b32 s11, v253, 37
	v_readlane_b32 s14, v253, 55
	s_nop 3
	s_add_u32 s12, s10, 0x6000
	s_addc_u32 s13, s11, 0
	s_and_b32 s15, s88, 7
	s_lshr_b32 s16, s88, 3
	s_lshl_b32 s15, s15, 3
	s_and_b32 s17, s16, 7
	s_add_i32 s17, s17, s15
	s_lshr_b32 s16, s16, 2
	s_add_i32 s16, s16, s15
	s_lshl_b32 s17, s17, 6
	s_lshl_b32 s16, s16, 6
	s_lshr_b32 s14, s14, 1
	s_add_i32 s14, s14, 1
	s_lshl_b32 s14, s14, 2
	v_mov_b32_e32 v2, s17
	v_mov_b32_e32 v5, 1
	v_mov_b32_e32 v4, s16
	global_atomic_add v2, v5, s[12:13]
	buffer_inv sc1
	s_mov_b32 s18, 0
.Lth_poll_LBB0_1745:
	global_load_dword v6, v4, s[12:13] sc1
	s_waitcnt vmcnt(0)
	v_cmp_gt_u32_e32 vcc, s14, v6
	s_nop 3
	s_cmp_eq_u64 vcc, 0
	s_cbranch_scc1 .Lth_done_LBB0_1745
	s_add_i32 s18, s18, 1
	s_cmp_gt_u32 s18, 0x4000
	s_cbranch_scc1 .Lth_done_LBB0_1745
	s_sleep 1
	s_branch .Lth_poll_LBB0_1745
.Lth_done_LBB0_1745:
	s_waitcnt vmcnt(0)
.LBB0_1745:
	s_or_b64 exec, exec, s[36:37]
	s_waitcnt lgkmcnt(0)
	s_barrier
